# speedup vs baseline: 1.0051x; 1.0006x over previous
_Z7gemm2_kILi3ELi2ELi2EEv5GArgs:
	v_lshlrev_b32_e32 v176, 4, v0
	s_getpc_b64 s[92:93]
	s_add_u32 s92, s92, 0xfffedbf8
	s_addc_u32 s93, s93, 0xffffffff
	global_load_dwordx4 v[172:175], v176, s[92:93]
	s_load_dwordx4 s[8:11], s[0:1], 0x48
	s_load_dwordx2 s[20:21], s[0:1], 0x58
	s_cmpk_lt_u32 s2, 0xc0
	s_mov_b64 s[4:5], -1
	s_cbranch_scc0 .LBB14_39
	s_lshl_b32 s4, s2, 3
	s_lshl_b32 s3, s2, 8
	s_and_b32 s28, s4, 0x780
	s_load_dwordx4 s[12:15], s[0:1], 0x30
	s_load_dwordx2 s[22:23], s[0:1], 0x18
	s_load_dwordx4 s[16:19], s[0:1], 0x0
	s_and_b32 s3, s3, 0xf00
	s_add_i32 s29, s28, 0xfffffd00
	s_cmpk_gt_u32 s2, 0x5f
	v_lshrrev_b32_e32 v136, 6, v0
	s_cselect_b64 s[26:27], -1, 0
	v_bfe_u32 v131, v0, 3, 3
	v_lshl_or_b32 v16, v136, 5, v131
	s_and_b64 s[6:7], s[26:27], exec
	s_cselect_b32 s4, 0xc00, 0
	v_or_b32_e32 v12, s3, v16
	s_waitcnt lgkmcnt(0)
	s_add_u32 s6, s16, s4
	v_mul_u32_u24_e32 v2, 0xc40, v12
	v_bfe_u32 v24, v0, 4, 2
	s_addc_u32 s7, s17, 0
	v_lshlrev_b32_e32 v34, 1, v2
	v_mov_b32_e32 v35, 0
	v_bitop3_b32 v4, v24, v0, 7 bitop3:0x78
	v_lshl_add_u64 v[2:3], s[6:7], 0, v[34:35]
	v_lshlrev_b32_e32 v4, 4, v4
	v_mov_b32_e32 v5, v35
	v_lshl_add_u64 v[2:3], v[2:3], 0, v[4:5]
	v_or_b32_e32 v5, 8, v16
	v_or_b32_e32 v6, s3, v5
	v_lshrrev_b32_e32 v5, 1, v5
	v_mul_u32_u24_e32 v6, 0xc40, v6
	v_mov_b32_e32 v7, v35
	v_xor_b32_e32 v10, v5, v0
	v_lshlrev_b64 v[6:7], 1, v[6:7]
	v_lshlrev_b32_e32 v10, 4, v10
	v_lshl_add_u64 v[8:9], s[6:7], 0, v[6:7]
	v_and_b32_e32 v10, 0x70, v10
	v_mov_b32_e32 v11, v35
	v_lshl_add_u64 v[8:9], v[8:9], 0, v[10:11]
	v_or_b32_e32 v10, 16, v12
	v_mul_u32_u24_e32 v10, 0xc40, v10
	v_lshlrev_b64 v[10:11], 1, v[10:11]
	v_lshl_add_u64 v[12:13], s[6:7], 0, v[10:11]
	v_xor_b32_e32 v14, 16, v4
	v_mov_b32_e32 v15, v35
	v_or_b32_e32 v18, 24, v16
	v_lshl_add_u64 v[12:13], v[12:13], 0, v[14:15]
	v_or_b32_e32 v14, s3, v18
	v_lshrrev_b32_e32 v18, 1, v18
	v_mul_u32_u24_e32 v14, 0xc40, v14
	v_xor_b32_e32 v18, v18, v0
	v_lshlrev_b64 v[14:15], 1, v[14:15]
	v_lshlrev_b32_e32 v18, 3, v18
	s_cmpk_lt_u32 s2, 0x60
	v_lshl_add_u64 v[16:17], s[6:7], 0, v[14:15]
	v_bitop3_b32 v18, v18, 8, 56 bitop3:0x6c
	s_cselect_b64 s[6:7], -1, 0
	v_lshlrev_b32_e32 v18, 1, v18
	v_mov_b32_e32 v19, v35
	s_and_b64 s[24:25], s[6:7], exec
	v_lshlrev_b32_e32 v83, 12, v136
	v_and_b32_e32 v20, 7, v0
	v_lshl_add_u64 v[16:17], v[16:17], 0, v[18:19]
	s_cselect_b32 s24, s28, s29
	v_lshl_or_b32 v19, v136, 4, v131
	v_readfirstlane_b32 s25, v83
	v_bitop3_b32 v30, v136, v20, 1 bitop3:0x6c
	v_or_b32_e32 v20, s24, v19
	s_mov_b32 m0, s25
	s_add_u32 s28, s18, s4
	v_mul_i32_i24_e32 v20, 0xc40, v20
	v_mov_b32_e32 v21, v35
	global_load_lds_dwordx4 v[2:3], off
	v_or_b32_e32 v2, 0x400, v83
	s_addc_u32 s29, s19, 0
	v_lshlrev_b64 v[20:21], 1, v[20:21]
	v_xor_b32_e32 v24, v30, v24
	v_readfirstlane_b32 s25, v2
	v_or_b32_e32 v2, 0x800, v83
	v_lshl_add_u64 v[22:23], s[28:29], 0, v[20:21]
	v_lshlrev_b32_e32 v24, 4, v24
	v_mov_b32_e32 v25, v35
	v_or_b32_e32 v19, 8, v19
	s_mov_b32 m0, s25
	v_readfirstlane_b32 s25, v2
	v_or_b32_e32 v2, 0xc00, v83
	v_lshl_add_u64 v[22:23], v[22:23], 0, v[24:25]
	v_or_b32_e32 v25, s24, v19
	global_load_lds_dwordx4 v[8:9], off
	s_mov_b32 m0, s25
	v_readfirstlane_b32 s25, v2
	v_lshlrev_b32_e32 v2, 11, v136
	v_mul_i32_i24_e32 v26, 0xc40, v25
	v_mov_b32_e32 v27, v35
	v_bfe_u32 v19, v19, 1, 3
	v_or_b32_e32 v85, 0x10000, v2
	v_lshlrev_b64 v[26:27], 1, v[26:27]
	v_xor_b32_e32 v19, v30, v19
	global_load_lds_dwordx4 v[12:13], off
	s_mov_b32 m0, s25
	v_readfirstlane_b32 s25, v85
	v_or_b32_e32 v2, 0x10400, v2
	v_lshl_add_u64 v[28:29], s[28:29], 0, v[26:27]
	v_lshlrev_b32_e32 v30, 4, v19
	v_mov_b32_e32 v31, v35
	global_load_lds_dwordx4 v[16:17], off
	s_mov_b32 m0, s25
	v_readfirstlane_b32 s25, v2
	v_lshl_add_u64 v[28:29], v[28:29], 0, v[30:31]
	global_load_lds_dwordx4 v[22:23], off
	s_mov_b32 m0, s25
	v_bfe_u32 v138, v0, 5, 1
	global_load_lds_dwordx4 v[28:29], off
	v_lshrrev_b32_e32 v2, 1, v0
	v_bfe_u32 v3, v0, 4, 1
	v_bitop3_b32 v2, v2, v3, 7 bitop3:0x6c
	v_or_b32_e32 v8, 2, v138
	v_xor_b32_e32 v8, v8, v2
	v_lshlrev_b32_e32 v84, 4, v8
	v_or_b32_e32 v8, 4, v138
	v_xor_b32_e32 v8, v8, v2
	v_lshrrev_b32_e32 v1, 7, v0
	v_xor_b32_e32 v3, v2, v138
	v_lshlrev_b32_e32 v82, 4, v8
	v_or_b32_e32 v8, 6, v138
	v_bfe_u32 v126, v0, 6, 1
	v_and_b32_e32 v139, 31, v0
	v_lshlrev_b32_e32 v3, 4, v3
	v_lshlrev_b32_e32 v80, 13, v1
	v_lshl_add_u32 v148, v1, 6, s3
	v_or_b32_e32 v148, v148, v131
	v_lshlrev_b32_e32 v148, 2, v148
	global_load_dword v147, v148, s[14:15]
	global_load_dword v146, v148, s[14:15] offset:32
	global_load_dword v145, v148, s[14:15] offset:64
	global_load_dword v144, v148, s[14:15] offset:96
	global_load_dword v142, v148, s[14:15] offset:128
	global_load_dword v141, v148, s[14:15] offset:160
	global_load_dword v140, v148, s[14:15] offset:192
	global_load_dword v130, v148, s[14:15] offset:224
	v_xor_b32_e32 v2, v8, v2
	v_lshlrev_b32_e32 v78, 7, v139
	v_lshlrev_b32_e32 v79, 13, v126
	v_lshlrev_b32_e32 v81, 4, v2
	v_or_b32_e32 v2, v3, v80
	v_add_u32_e32 v86, v2, v78
	v_or3_b32 v2, v3, v79, v78
	v_add_u32_e32 v87, 0x10000, v2
	v_or_b32_e32 v2, s4, v4
	v_mov_b32_e32 v3, v35
	v_lshl_add_u64 v[2:3], v[2:3], 0, v[34:35]
	v_lshl_add_u64 v[2:3], s[16:17], 0, v[2:3]
	s_mov_b64 s[28:29], 0x80
	v_lshl_add_u64 v[66:67], v[2:3], 0, s[28:29]
	v_bitop3_b32 v2, v5, 7, v0 bitop3:0x48
	v_lshl_or_b32 v34, v2, 4, s4
	v_lshl_add_u64 v[2:3], v[34:35], 0, v[6:7]
	s_mov_b32 s5, 0
	v_lshl_add_u64 v[2:3], s[16:17], 0, v[2:3]
	v_lshl_add_u64 v[68:69], v[2:3], 0, s[28:29]
	v_lshl_add_u64 v[2:3], s[4:5], 0, v[10:11]
	v_bitop3_b32 v2, v2, v4, 16 bitop3:0xf6
	v_lshl_add_u64 v[2:3], s[16:17], 0, v[2:3]
	v_lshl_add_u64 v[70:71], v[2:3], 0, s[28:29]
	v_lshl_add_u64 v[2:3], s[4:5], 0, v[14:15]
	v_or_b32_e32 v2, v2, v18
	v_lshl_add_u64 v[2:3], s[16:17], 0, v[2:3]
	v_or_b32_e32 v34, s4, v24
	v_lshl_add_u64 v[72:73], v[2:3], 0, s[28:29]
	v_lshl_add_u64 v[2:3], v[34:35], 0, v[20:21]
	v_lshl_add_u64 v[2:3], s[18:19], 0, v[2:3]
	v_or_b32_e32 v34, s4, v30
	s_waitcnt vmcnt(0)
	v_lshl_add_u64 v[74:75], v[2:3], 0, s[28:29]
	v_lshl_add_u64 v[2:3], v[34:35], 0, v[26:27]
	v_lshl_add_u64 v[2:3], s[18:19], 0, v[2:3]
	v_lshl_add_u64 v[76:77], v[2:3], 0, s[28:29]
	s_mov_b64 s[16:17], 0
	v_mov_b32_e32 v88, 0x8000
	v_mov_b32_e32 v34, v35
	v_mov_b32_e32 v36, v35
	v_mov_b32_e32 v37, v35
	v_mov_b32_e32 v38, v35
	v_mov_b32_e32 v39, v35
	v_mov_b32_e32 v40, v35
	v_mov_b32_e32 v41, v35
	v_mov_b32_e32 v42, v35
	v_mov_b32_e32 v43, v35
	v_mov_b32_e32 v44, v35
	v_mov_b32_e32 v45, v35
	v_mov_b32_e32 v46, v35
	v_mov_b32_e32 v47, v35
	v_mov_b32_e32 v48, v35
	v_mov_b32_e32 v49, v35
	v_mov_b32_e32 v50, v35
	v_mov_b32_e32 v51, v35
	v_mov_b32_e32 v52, v35
	v_mov_b32_e32 v53, v35
	v_mov_b32_e32 v54, v35
	v_mov_b32_e32 v55, v35
	v_mov_b32_e32 v56, v35
	v_mov_b32_e32 v57, v35
	v_mov_b32_e32 v58, v35
	v_mov_b32_e32 v59, v35
	v_mov_b32_e32 v60, v35
	v_mov_b32_e32 v61, v35
	v_mov_b32_e32 v62, v35
	v_mov_b32_e32 v63, v35
	v_mov_b32_e32 v64, v35
	v_mov_b32_e32 v65, v35
	v_mov_b32_e32 v18, v35
	v_mov_b32_e32 v19, v35
	v_mov_b32_e32 v20, v35
	v_mov_b32_e32 v21, v35
	v_mov_b32_e32 v22, v35
	v_mov_b32_e32 v23, v35
	v_mov_b32_e32 v24, v35
	v_mov_b32_e32 v25, v35
	v_mov_b32_e32 v26, v35
	v_mov_b32_e32 v27, v35
	v_mov_b32_e32 v28, v35
	v_mov_b32_e32 v29, v35
	v_mov_b32_e32 v30, v35
	v_mov_b32_e32 v32, v35
	v_mov_b32_e32 v33, v35
	v_mov_b32_e32 v2, v35
	v_mov_b32_e32 v3, v35
	v_mov_b32_e32 v4, v35
	v_mov_b32_e32 v5, v35
	v_mov_b32_e32 v6, v35
	v_mov_b32_e32 v7, v35
	v_mov_b32_e32 v8, v35
	v_mov_b32_e32 v9, v35
	v_mov_b32_e32 v10, v35
	v_mov_b32_e32 v11, v35
	v_mov_b32_e32 v12, v35
	v_mov_b32_e32 v13, v35
	v_mov_b32_e32 v14, v35
	v_mov_b32_e32 v15, v35
	v_mov_b32_e32 v16, v35
	v_mov_b32_e32 v17, v35
	s_waitcnt vmcnt(0) lgkmcnt(0)
	s_barrier
.LBB14_2:
	s_and_b32 s4, s5, 1
	s_lshl_b32 s18, s4, 15
	v_bitop3_b32 v89, v83, s18, v88 bitop3:0xf6
	v_add_u32_e32 v92, 0x400, v89
	v_readfirstlane_b32 s19, v89
	v_lshl_add_u64 v[90:91], v[66:67], 0, s[16:17]
	s_mov_b32 m0, s19
	v_readfirstlane_b32 s19, v92
	v_add_u32_e32 v92, 0x800, v89
	global_load_lds_dwordx4 v[90:91], off
	v_lshl_add_u64 v[90:91], v[68:69], 0, s[16:17]
	s_mov_b32 m0, s19
	v_readfirstlane_b32 s19, v92
	v_add_u32_e32 v89, 0xc00, v89
	global_load_lds_dwordx4 v[90:91], off
	v_lshl_add_u64 v[90:91], v[70:71], 0, s[16:17]
	s_mov_b32 m0, s19
	v_readfirstlane_b32 s19, v89
	s_lshl_b32 s4, s4, 14
	global_load_lds_dwordx4 v[90:91], off
	s_mov_b32 m0, s19
	s_xor_b32 s19, s4, 0x4000
	v_add_u32_e32 v89, s19, v85
	v_lshl_add_u64 v[90:91], v[72:73], 0, s[16:17]
	v_readfirstlane_b32 s19, v89
	v_add_u32_e32 v89, 0x400, v89
	global_load_lds_dwordx4 v[90:91], off
	v_lshl_add_u64 v[90:91], v[74:75], 0, s[16:17]
	s_mov_b32 m0, s19
	v_readfirstlane_b32 s19, v89
	global_load_lds_dwordx4 v[90:91], off
	v_lshl_add_u64 v[90:91], v[76:77], 0, s[16:17]
	s_mov_b32 m0, s19
	s_add_i32 s5, s5, 1
	global_load_lds_dwordx4 v[90:91], off
	v_add_u32_e32 v89, s18, v86
	ds_read_b128 v[90:93], v89
	v_add_u32_e32 v102, s4, v87
	ds_read_b128 v[94:97], v102
	ds_read_b128 v[98:101], v89 offset:4096
	ds_read_b128 v[102:105], v102 offset:4096
	v_or_b32_e32 v89, s18, v84
	s_bitset1_b32 s4, 16
	s_waitcnt lgkmcnt(0)
	v_mfma_f32_32x32x16_f16 v[18:33], v[98:101], v[94:97], v[18:33]
	v_add3_u32 v89, v89, v80, v78
	v_mfma_f32_32x32x16_f16 v[34:49], v[90:93], v[94:97], v[34:49]
	v_mfma_f32_32x32x16_f16 v[50:65], v[90:93], v[102:105], v[50:65]
	ds_read_b128 v[90:93], v89
	ds_read_b128 v[94:97], v89 offset:4096
	v_or_b32_e32 v89, s4, v84
	v_add3_u32 v89, v89, v79, v78
	ds_read_b128 v[106:109], v89
	ds_read_b128 v[110:113], v89 offset:4096
	v_mfma_f32_32x32x16_f16 v[2:17], v[98:101], v[102:105], v[2:17]
	v_or_b32_e32 v89, s18, v82
	s_waitcnt lgkmcnt(0)
	v_mfma_f32_32x32x16_f16 v[34:49], v[90:93], v[106:109], v[34:49]
	v_add3_u32 v89, v89, v80, v78
	v_mfma_f32_32x32x16_f16 v[50:65], v[90:93], v[110:113], v[50:65]
	ds_read_b128 v[90:93], v89
	ds_read_b128 v[98:101], v89 offset:4096
	v_or_b32_e32 v89, s4, v82
	v_add3_u32 v89, v89, v79, v78
	v_mfma_f32_32x32x16_f16 v[18:33], v[94:97], v[106:109], v[18:33]
	ds_read_b128 v[102:105], v89
	ds_read_b128 v[106:109], v89 offset:4096
	v_mfma_f32_32x32x16_f16 v[2:17], v[94:97], v[110:113], v[2:17]
	v_or_b32_e32 v89, s18, v81
	s_waitcnt lgkmcnt(0)
	v_mfma_f32_32x32x16_f16 v[34:49], v[90:93], v[102:105], v[34:49]
	v_add3_u32 v89, v89, v80, v78
	v_mfma_f32_32x32x16_f16 v[50:65], v[90:93], v[106:109], v[50:65]
	ds_read_b128 v[90:93], v89
	ds_read_b128 v[94:97], v89 offset:4096
	v_or_b32_e32 v89, s4, v81
	v_add3_u32 v89, v89, v79, v78
	v_mfma_f32_32x32x16_f16 v[18:33], v[98:101], v[102:105], v[18:33]
	ds_read_b128 v[102:105], v89
	ds_read_b128 v[110:113], v89 offset:4096
	v_mfma_f32_32x32x16_f16 v[2:17], v[98:101], v[106:109], v[2:17]
	s_waitcnt lgkmcnt(0)
	v_mfma_f32_32x32x16_f16 v[34:49], v[90:93], v[102:105], v[34:49]
	v_mfma_f32_32x32x16_f16 v[50:65], v[90:93], v[110:113], v[50:65]
	v_mfma_f32_32x32x16_f16 v[18:33], v[94:97], v[102:105], v[18:33]
	v_mfma_f32_32x32x16_f16 v[2:17], v[94:97], v[110:113], v[2:17]
	s_waitcnt vmcnt(0)
	s_add_u32 s16, s16, 0x80
	s_addc_u32 s17, s17, 0
	s_cmpk_eq_i32 s16, 0xb80
	s_waitcnt vmcnt(0)
	s_barrier
	s_cbranch_scc0 .LBB14_2
	ds_read_b128 v[66:69], v86 offset:32768
	ds_read_b128 v[70:73], v87 offset:16384
	ds_read_b128 v[74:77], v86 offset:36864
	ds_read_b128 v[86:89], v87 offset:20480
	v_add3_u32 v83, v84, v80, v78
	s_mov_b32 s4, 0x14000
	s_waitcnt lgkmcnt(2)
	v_mfma_f32_32x32x16_f16 v[34:49], v[66:69], v[70:73], v[34:49]
	s_waitcnt lgkmcnt(0)
	v_mfma_f32_32x32x16_f16 v[50:65], v[66:69], v[86:89], v[50:65]
	v_mfma_f32_32x32x16_f16 v[18:33], v[74:77], v[70:73], v[18:33]
	ds_read_b128 v[66:69], v83 offset:32768
	ds_read_b128 v[70:73], v83 offset:36864
	v_add_u32_e32 v83, v79, v84
	v_add3_u32 v83, v83, v78, s4
	ds_read_b128 v[90:93], v83
	ds_read_b128 v[94:97], v83 offset:4096
	v_mfma_f32_32x32x16_f16 v[2:17], v[74:77], v[86:89], v[2:17]
	s_waitcnt lgkmcnt(1)
	v_mfma_f32_32x32x16_f16 v[34:49], v[66:69], v[90:93], v[34:49]
	v_add3_u32 v74, v82, v80, v78
	v_add_u32_e32 v82, v79, v82
	v_add3_u32 v86, v82, v78, s4
	s_waitcnt lgkmcnt(0)
	v_mfma_f32_32x32x16_f16 v[50:65], v[66:69], v[94:97], v[50:65]
	ds_read_b128 v[66:69], v74 offset:32768
	ds_read_b128 v[74:77], v74 offset:36864
	ds_read_b128 v[82:85], v86
	ds_read_b128 v[86:89], v86 offset:4096
	v_mfma_f32_32x32x16_f16 v[18:33], v[70:73], v[90:93], v[18:33]
	v_mfma_f32_32x32x16_f16 v[2:17], v[70:73], v[94:97], v[2:17]
	s_waitcnt lgkmcnt(1)
	v_mfma_f32_32x32x16_f16 v[34:49], v[66:69], v[82:85], v[34:49]
	v_add_u32_e32 v79, v79, v81
	v_add3_u32 v70, v81, v80, v78
	s_waitcnt lgkmcnt(0)
	v_mfma_f32_32x32x16_f16 v[50:65], v[66:69], v[86:89], v[50:65]
	ds_read_b128 v[66:69], v70 offset:32768
	ds_read_b128 v[70:73], v70 offset:36864
	v_mfma_f32_32x32x16_f16 v[18:33], v[74:77], v[82:85], v[18:33]
	v_add3_u32 v82, v79, v78, s4
	ds_read_b128 v[78:81], v82
	ds_read_b128 v[82:85], v82 offset:4096
	v_mfma_f32_32x32x16_f16 v[2:17], v[74:77], v[86:89], v[2:17]
	s_waitcnt lgkmcnt(1)
	v_mfma_f32_32x32x16_f16 v[34:49], v[66:69], v[78:81], v[34:49]
	s_waitcnt lgkmcnt(0)
	v_mfma_f32_32x32x16_f16 v[50:65], v[66:69], v[82:85], v[50:65]
	v_mfma_f32_32x32x16_f16 v[18:33], v[70:73], v[78:81], v[18:33]
	v_mfma_f32_32x32x16_f16 v[2:17], v[70:73], v[82:85], v[2:17]
	s_waitcnt vmcnt(0)
	s_barrier
	s_mov_b32 s25, 0
	s_lshl_b64 s[4:5], s[24:25], 2
	s_add_u32 s4, s12, s4
	v_lshlrev_b32_e32 v1, 2, v0
	s_addc_u32 s5, s13, s5
	v_lshlrev_b32_e32 v132, 8, v126
	v_mov_b32_e32 v133, 0
	v_and_b32_e32 v143, 28, v1
	v_lshl_add_u64 v[66:67], s[4:5], 0, v[132:133]
	v_lshlrev_b32_e32 v132, 2, v143
	v_lshl_add_u64 v[134:135], v[66:67], 0, v[132:133]
	s_and_b64 vcc, s[6:7], exec
	v_mov_b32_e32 v90, 0
	v_mov_b32_e32 v91, 0
	v_mov_b32_e32 v92, 0
	v_mov_b32_e32 v93, 0
	s_cbranch_vccz .LBB14_5
	s_movk_i32 s3, 0xc00
	s_waitcnt vmcnt(7)
	v_mad_i64_i32 v[66:67], s[4:5], v147, s3, v[134:135]
	global_load_dwordx4 v[90:93], v[66:67], off
